# expert-weight converter stores its e4m3 output with sc1 (write-through: 400 MB that nothing re-reads before P9 no longer displace the in-proj GEMM operands in L2)
# speedup vs baseline: 1.0018x; 1.0018x over previous
.Lcv_ld_3:
	s_add_u32 s2, s2, s3
	v_cndmask_b32_e32 v246, v245, v244, vcc
	global_load_dwordx4 v[0:3], v246, s[4:5] nt
	s_add_u32 s4, s4, s14
	s_addc_u32 s5, s5, 0
	global_load_dwordx4 v[4:7], v246, s[4:5] nt
	s_add_u32 s4, s4, s14
	s_addc_u32 s5, s5, 0
	global_load_dwordx4 v[8:11], v246, s[4:5] nt
	s_add_u32 s4, s4, s14
	s_addc_u32 s5, s5, 0
	global_load_dwordx4 v[12:15], v246, s[4:5] nt
	s_add_u32 s4, s4, s14
	s_addc_u32 s5, s5, 0
	global_load_dwordx4 v[16:19], v246, s[4:5] nt
	s_add_u32 s4, s4, s14
	s_addc_u32 s5, s5, 0
	global_load_dwordx4 v[20:23], v246, s[4:5] nt
	s_add_u32 s4, s4, s14
	s_addc_u32 s5, s5, 0
	global_load_dwordx4 v[24:27], v246, s[4:5] nt
	s_add_u32 s4, s4, s14
	s_addc_u32 s5, s5, 0
	global_load_dwordx4 v[28:31], v246, s[4:5] nt
	s_add_u32 s4, s4, s14
	s_addc_u32 s5, s5, 0
	global_load_dwordx4 v[32:35], v246, s[4:5] nt
	s_add_u32 s4, s4, s14
	s_addc_u32 s5, s5, 0
	global_load_dwordx4 v[36:39], v246, s[4:5] nt
	s_add_u32 s4, s4, s14
	s_addc_u32 s5, s5, 0
	global_load_dwordx4 v[40:43], v246, s[4:5] nt
	s_add_u32 s4, s4, s14
	s_addc_u32 s5, s5, 0
	global_load_dwordx4 v[44:47], v246, s[4:5] nt
	s_add_u32 s4, s4, s14
	s_addc_u32 s5, s5, 0
	global_load_dwordx4 v[48:51], v246, s[4:5] nt
	s_add_u32 s4, s4, s14
	s_addc_u32 s5, s5, 0
	global_load_dwordx4 v[52:55], v246, s[4:5] nt
	s_add_u32 s4, s4, s14
	s_addc_u32 s5, s5, 0
	global_load_dwordx4 v[56:59], v246, s[4:5] nt
	s_add_u32 s4, s4, s14
	s_addc_u32 s5, s5, 0
	global_load_dwordx4 v[60:63], v246, s[4:5] nt
	ds_write_b32 v247, v192 offset:0
	ds_write_b32 v247, v193 offset:32
	ds_write_b32 v247, v194 offset:64
	ds_write_b32 v247, v195 offset:96
	ds_write_b32 v247, v196 offset:128
	ds_write_b32 v247, v197 offset:160
	ds_write_b32 v247, v198 offset:192
	ds_write_b32 v247, v199 offset:224
	ds_write_b32 v247, v200 offset:256
	ds_write_b32 v247, v201 offset:288
	ds_write_b32 v247, v202 offset:320
	ds_write_b32 v247, v203 offset:352
	ds_write_b32 v247, v204 offset:384
	ds_write_b32 v247, v205 offset:416
	ds_write_b32 v247, v206 offset:448
	ds_write_b32 v247, v207 offset:480
	ds_read_b128 v[208:211], v248 offset:0
	ds_read_b128 v[212:215], v248 offset:16
	ds_read_b128 v[216:219], v248 offset:32
	ds_read_b128 v[220:223], v248 offset:48
	s_waitcnt lgkmcnt(3)
	v_perm_b32 v240, v209, v208, s16
	v_perm_b32 v241, v209, v208, s17
	v_perm_b32 v242, v211, v210, s16
	v_perm_b32 v243, v211, v210, s17
	v_perm_b32 v224, v242, v240, s18
	v_perm_b32 v228, v242, v240, s19
	v_perm_b32 v232, v243, v241, s18
	v_perm_b32 v236, v243, v241, s19
	s_waitcnt lgkmcnt(2)
	v_perm_b32 v240, v213, v212, s16
	v_perm_b32 v241, v213, v212, s17
	v_perm_b32 v242, v215, v214, s16
	v_perm_b32 v243, v215, v214, s17
	v_perm_b32 v225, v242, v240, s18
	v_perm_b32 v229, v242, v240, s19
	v_perm_b32 v233, v243, v241, s18
	v_perm_b32 v237, v243, v241, s19
	s_waitcnt lgkmcnt(1)
	v_perm_b32 v240, v217, v216, s16
	v_perm_b32 v241, v217, v216, s17
	v_perm_b32 v242, v219, v218, s16
	v_perm_b32 v243, v219, v218, s17
	v_perm_b32 v226, v242, v240, s18
	v_perm_b32 v230, v242, v240, s19
	v_perm_b32 v234, v243, v241, s18
	v_perm_b32 v238, v243, v241, s19
	s_waitcnt lgkmcnt(0)
	v_perm_b32 v240, v221, v220, s16
	v_perm_b32 v241, v221, v220, s17
	v_perm_b32 v242, v223, v222, s16
	v_perm_b32 v243, v223, v222, s17
	v_perm_b32 v227, v242, v240, s18
	v_perm_b32 v231, v242, v240, s19
	v_perm_b32 v235, v243, v241, s18
	v_perm_b32 v239, v243, v241, s19
	s_add_u32 s26, s6, 0x1000
	s_addc_u32 s27, s7, 0
	global_store_dwordx4 v249, v[224:227], s[6:7] sc1
	global_store_dwordx4 v249, v[228:231], s[6:7] offset:2048 sc1
	global_store_dwordx4 v249, v[232:235], s[26:27] sc1
	global_store_dwordx4 v249, v[236:239], s[26:27] offset:2048 sc1
	s_mov_b64 s[6:7], s[20:21]
	s_waitcnt vmcnt(36)
	v_mul_f32_e32 v64, 0x42800000, v64
	v_mul_f32_e32 v65, 0x42800000, v65
	v_mul_f32_e32 v66, 0x42800000, v66
	v_mul_f32_e32 v67, 0x42800000, v67
	v_med3_f32 v64, v64, s15, v250
	v_med3_f32 v65, v65, s15, v250
	v_med3_f32 v66, v66, s15, v250
	v_med3_f32 v67, v67, s15, v250
	v_cvt_pk_fp8_f32 v192, v64, v65
	v_cvt_pk_fp8_f32 v192, v66, v67 op_sel:[0,0,1]
	v_mul_f32_e32 v68, 0x42800000, v68
	v_mul_f32_e32 v69, 0x42800000, v69
	v_mul_f32_e32 v70, 0x42800000, v70
	v_mul_f32_e32 v71, 0x42800000, v71
	v_med3_f32 v68, v68, s15, v250
	v_med3_f32 v69, v69, s15, v250
	v_med3_f32 v70, v70, s15, v250
	v_med3_f32 v71, v71, s15, v250
	v_cvt_pk_fp8_f32 v193, v68, v69
	v_cvt_pk_fp8_f32 v193, v70, v71 op_sel:[0,0,1]
	v_mul_f32_e32 v72, 0x42800000, v72
	v_mul_f32_e32 v73, 0x42800000, v73
	v_mul_f32_e32 v74, 0x42800000, v74
	v_mul_f32_e32 v75, 0x42800000, v75
	v_med3_f32 v72, v72, s15, v250
	v_med3_f32 v73, v73, s15, v250
	v_med3_f32 v74, v74, s15, v250
	v_med3_f32 v75, v75, s15, v250
	v_cvt_pk_fp8_f32 v194, v72, v73
	v_cvt_pk_fp8_f32 v194, v74, v75 op_sel:[0,0,1]
	v_mul_f32_e32 v76, 0x42800000, v76
	v_mul_f32_e32 v77, 0x42800000, v77
	v_mul_f32_e32 v78, 0x42800000, v78
	v_mul_f32_e32 v79, 0x42800000, v79
	v_med3_f32 v76, v76, s15, v250
	v_med3_f32 v77, v77, s15, v250
	v_med3_f32 v78, v78, s15, v250
	v_med3_f32 v79, v79, s15, v250
	v_cvt_pk_fp8_f32 v195, v76, v77
	v_cvt_pk_fp8_f32 v195, v78, v79 op_sel:[0,0,1]
	v_mul_f32_e32 v80, 0x42800000, v80
	v_mul_f32_e32 v81, 0x42800000, v81
	v_mul_f32_e32 v82, 0x42800000, v82
	v_mul_f32_e32 v83, 0x42800000, v83
	v_med3_f32 v80, v80, s15, v250
	v_med3_f32 v81, v81, s15, v250
	v_med3_f32 v82, v82, s15, v250
	v_med3_f32 v83, v83, s15, v250
	v_cvt_pk_fp8_f32 v196, v80, v81
	v_cvt_pk_fp8_f32 v196, v82, v83 op_sel:[0,0,1]
	v_mul_f32_e32 v84, 0x42800000, v84
	v_mul_f32_e32 v85, 0x42800000, v85
	v_mul_f32_e32 v86, 0x42800000, v86
	v_mul_f32_e32 v87, 0x42800000, v87
	v_med3_f32 v84, v84, s15, v250
	v_med3_f32 v85, v85, s15, v250
	v_med3_f32 v86, v86, s15, v250
	v_med3_f32 v87, v87, s15, v250
	v_cvt_pk_fp8_f32 v197, v84, v85
	v_cvt_pk_fp8_f32 v197, v86, v87 op_sel:[0,0,1]
	v_mul_f32_e32 v88, 0x42800000, v88
	v_mul_f32_e32 v89, 0x42800000, v89
	v_mul_f32_e32 v90, 0x42800000, v90
	v_mul_f32_e32 v91, 0x42800000, v91
	v_med3_f32 v88, v88, s15, v250
	v_med3_f32 v89, v89, s15, v250
	v_med3_f32 v90, v90, s15, v250
	v_med3_f32 v91, v91, s15, v250
	v_cvt_pk_fp8_f32 v198, v88, v89
	v_cvt_pk_fp8_f32 v198, v90, v91 op_sel:[0,0,1]
	v_mul_f32_e32 v92, 0x42800000, v92
	v_mul_f32_e32 v93, 0x42800000, v93
	v_mul_f32_e32 v94, 0x42800000, v94
	v_mul_f32_e32 v95, 0x42800000, v95
	v_med3_f32 v92, v92, s15, v250
	v_med3_f32 v93, v93, s15, v250
	v_med3_f32 v94, v94, s15, v250
	v_med3_f32 v95, v95, s15, v250
	v_cvt_pk_fp8_f32 v199, v92, v93
	v_cvt_pk_fp8_f32 v199, v94, v95 op_sel:[0,0,1]
	v_mul_f32_e32 v96, 0x42800000, v96
	v_mul_f32_e32 v97, 0x42800000, v97
	v_mul_f32_e32 v98, 0x42800000, v98
	v_mul_f32_e32 v99, 0x42800000, v99
	v_med3_f32 v96, v96, s15, v250
	v_med3_f32 v97, v97, s15, v250
	v_med3_f32 v98, v98, s15, v250
	v_med3_f32 v99, v99, s15, v250
	v_cvt_pk_fp8_f32 v200, v96, v97
	v_cvt_pk_fp8_f32 v200, v98, v99 op_sel:[0,0,1]
	v_mul_f32_e32 v100, 0x42800000, v100
	v_mul_f32_e32 v101, 0x42800000, v101
	v_mul_f32_e32 v102, 0x42800000, v102
	v_mul_f32_e32 v103, 0x42800000, v103
	v_med3_f32 v100, v100, s15, v250
	v_med3_f32 v101, v101, s15, v250
	v_med3_f32 v102, v102, s15, v250
	v_med3_f32 v103, v103, s15, v250
	v_cvt_pk_fp8_f32 v201, v100, v101
	v_cvt_pk_fp8_f32 v201, v102, v103 op_sel:[0,0,1]
	v_mul_f32_e32 v104, 0x42800000, v104
	v_mul_f32_e32 v105, 0x42800000, v105
	v_mul_f32_e32 v106, 0x42800000, v106
	v_mul_f32_e32 v107, 0x42800000, v107
	v_med3_f32 v104, v104, s15, v250
	v_med3_f32 v105, v105, s15, v250
	v_med3_f32 v106, v106, s15, v250
	v_med3_f32 v107, v107, s15, v250
	v_cvt_pk_fp8_f32 v202, v104, v105
	v_cvt_pk_fp8_f32 v202, v106, v107 op_sel:[0,0,1]
	v_mul_f32_e32 v108, 0x42800000, v108
	v_mul_f32_e32 v109, 0x42800000, v109
	v_mul_f32_e32 v110, 0x42800000, v110
	v_mul_f32_e32 v111, 0x42800000, v111
	v_med3_f32 v108, v108, s15, v250
	v_med3_f32 v109, v109, s15, v250
	v_med3_f32 v110, v110, s15, v250
	v_med3_f32 v111, v111, s15, v250
	v_cvt_pk_fp8_f32 v203, v108, v109
	v_cvt_pk_fp8_f32 v203, v110, v111 op_sel:[0,0,1]
	v_mul_f32_e32 v112, 0x42800000, v112
	v_mul_f32_e32 v113, 0x42800000, v113
	v_mul_f32_e32 v114, 0x42800000, v114
	v_mul_f32_e32 v115, 0x42800000, v115
	v_med3_f32 v112, v112, s15, v250
	v_med3_f32 v113, v113, s15, v250
	v_med3_f32 v114, v114, s15, v250
	v_med3_f32 v115, v115, s15, v250
	v_cvt_pk_fp8_f32 v204, v112, v113
	v_cvt_pk_fp8_f32 v204, v114, v115 op_sel:[0,0,1]
	v_mul_f32_e32 v116, 0x42800000, v116
	v_mul_f32_e32 v117, 0x42800000, v117
	v_mul_f32_e32 v118, 0x42800000, v118
	v_mul_f32_e32 v119, 0x42800000, v119
	v_med3_f32 v116, v116, s15, v250
	v_med3_f32 v117, v117, s15, v250
	v_med3_f32 v118, v118, s15, v250
	v_med3_f32 v119, v119, s15, v250
	v_cvt_pk_fp8_f32 v205, v116, v117
	v_cvt_pk_fp8_f32 v205, v118, v119 op_sel:[0,0,1]
	v_mul_f32_e32 v120, 0x42800000, v120
	v_mul_f32_e32 v121, 0x42800000, v121
	v_mul_f32_e32 v122, 0x42800000, v122
	v_mul_f32_e32 v123, 0x42800000, v123
	v_med3_f32 v120, v120, s15, v250
	v_med3_f32 v121, v121, s15, v250
	v_med3_f32 v122, v122, s15, v250
	v_med3_f32 v123, v123, s15, v250
	v_cvt_pk_fp8_f32 v206, v120, v121
	v_cvt_pk_fp8_f32 v206, v122, v123 op_sel:[0,0,1]
	v_mul_f32_e32 v124, 0x42800000, v124
	v_mul_f32_e32 v125, 0x42800000, v125
	v_mul_f32_e32 v126, 0x42800000, v126
	v_mul_f32_e32 v127, 0x42800000, v127
	v_med3_f32 v124, v124, s15, v250
	v_med3_f32 v125, v125, s15, v250
	v_med3_f32 v126, v126, s15, v250
	v_med3_f32 v127, v127, s15, v250
	v_cvt_pk_fp8_f32 v207, v124, v125
	v_cvt_pk_fp8_f32 v207, v126, v127 op_sel:[0,0,1]
	s_min_u32 s22, s2, s28
	s_cmp_lt_u32 s22, 0x10000
	s_cbranch_scc0 .Lcv_dn_4
	s_lshr_b32 s23, s22, 11
	s_bfe_u32 s24, s22, 0x40007
	s_and_b32 s25, s22, 0x7f
	s_lshl_b32 s30, s24, 7
	s_lshl_b32 s24, s24, 21
	s_lshl_b32 s22, s25, 7
	s_add_u32 s24, s24, s22
	s_lshl_b32 s25, s25, 16
	s_add_u32 s30, s30, s25
	s_lshl_b32 s22, s23, 25
	s_add_u32 s24, s24, s22
	s_add_u32 s4, s70, s24
	s_addc_u32 s5, s71, 0
	s_lshl_b32 s23, s23, 23
	s_add_u32 s30, s30, s23
	s_add_u32 s30, s30, 0x38ee1c00
	s_add_u32 s20, s92, s30
	s_addc_u32 s21, s93, 0
	s_mov_b32 s14, 0x20000
	s_mov_b64 vcc, -1
	s_branch .Lcv_ld_4

.Lcv_ld_4:
	s_add_u32 s2, s2, s3
	v_cndmask_b32_e32 v246, v245, v244, vcc
	global_load_dwordx4 v[64:67], v246, s[4:5] nt
	s_add_u32 s4, s4, s14
	s_addc_u32 s5, s5, 0
	global_load_dwordx4 v[68:71], v246, s[4:5] nt
	s_add_u32 s4, s4, s14
	s_addc_u32 s5, s5, 0
	global_load_dwordx4 v[72:75], v246, s[4:5] nt
	s_add_u32 s4, s4, s14
	s_addc_u32 s5, s5, 0
	global_load_dwordx4 v[76:79], v246, s[4:5] nt
	s_add_u32 s4, s4, s14
	s_addc_u32 s5, s5, 0
	global_load_dwordx4 v[80:83], v246, s[4:5] nt
	s_add_u32 s4, s4, s14
	s_addc_u32 s5, s5, 0
	global_load_dwordx4 v[84:87], v246, s[4:5] nt
	s_add_u32 s4, s4, s14
	s_addc_u32 s5, s5, 0
	global_load_dwordx4 v[88:91], v246, s[4:5] nt
	s_add_u32 s4, s4, s14
	s_addc_u32 s5, s5, 0
	global_load_dwordx4 v[92:95], v246, s[4:5] nt
	s_add_u32 s4, s4, s14
	s_addc_u32 s5, s5, 0
	global_load_dwordx4 v[96:99], v246, s[4:5] nt
	s_add_u32 s4, s4, s14
	s_addc_u32 s5, s5, 0
	global_load_dwordx4 v[100:103], v246, s[4:5] nt
	s_add_u32 s4, s4, s14
	s_addc_u32 s5, s5, 0
	global_load_dwordx4 v[104:107], v246, s[4:5] nt
	s_add_u32 s4, s4, s14
	s_addc_u32 s5, s5, 0
	global_load_dwordx4 v[108:111], v246, s[4:5] nt
	s_add_u32 s4, s4, s14
	s_addc_u32 s5, s5, 0
	global_load_dwordx4 v[112:115], v246, s[4:5] nt
	s_add_u32 s4, s4, s14
	s_addc_u32 s5, s5, 0
	global_load_dwordx4 v[116:119], v246, s[4:5] nt
	s_add_u32 s4, s4, s14
	s_addc_u32 s5, s5, 0
	global_load_dwordx4 v[120:123], v246, s[4:5] nt
	s_add_u32 s4, s4, s14
	s_addc_u32 s5, s5, 0
	global_load_dwordx4 v[124:127], v246, s[4:5] nt
	ds_write_b32 v247, v192 offset:0
	ds_write_b32 v247, v193 offset:32
	ds_write_b32 v247, v194 offset:64
	ds_write_b32 v247, v195 offset:96
	ds_write_b32 v247, v196 offset:128
	ds_write_b32 v247, v197 offset:160
	ds_write_b32 v247, v198 offset:192
	ds_write_b32 v247, v199 offset:224
	ds_write_b32 v247, v200 offset:256
	ds_write_b32 v247, v201 offset:288
	ds_write_b32 v247, v202 offset:320
	ds_write_b32 v247, v203 offset:352
	ds_write_b32 v247, v204 offset:384
	ds_write_b32 v247, v205 offset:416
	ds_write_b32 v247, v206 offset:448
	ds_write_b32 v247, v207 offset:480
	ds_read_b128 v[208:211], v248 offset:0
	ds_read_b128 v[212:215], v248 offset:16
	ds_read_b128 v[216:219], v248 offset:32
	ds_read_b128 v[220:223], v248 offset:48
	s_waitcnt lgkmcnt(3)
	v_perm_b32 v240, v209, v208, s16
	v_perm_b32 v241, v209, v208, s17
	v_perm_b32 v242, v211, v210, s16
	v_perm_b32 v243, v211, v210, s17
	v_perm_b32 v224, v242, v240, s18
	v_perm_b32 v228, v242, v240, s19
	v_perm_b32 v232, v243, v241, s18
	v_perm_b32 v236, v243, v241, s19
	s_waitcnt lgkmcnt(2)
	v_perm_b32 v240, v213, v212, s16
	v_perm_b32 v241, v213, v212, s17
	v_perm_b32 v242, v215, v214, s16
	v_perm_b32 v243, v215, v214, s17
	v_perm_b32 v225, v242, v240, s18
	v_perm_b32 v229, v242, v240, s19
	v_perm_b32 v233, v243, v241, s18
	v_perm_b32 v237, v243, v241, s19
	s_waitcnt lgkmcnt(1)
	v_perm_b32 v240, v217, v216, s16
	v_perm_b32 v241, v217, v216, s17
	v_perm_b32 v242, v219, v218, s16
	v_perm_b32 v243, v219, v218, s17
	v_perm_b32 v226, v242, v240, s18
	v_perm_b32 v230, v242, v240, s19
	v_perm_b32 v234, v243, v241, s18
	v_perm_b32 v238, v243, v241, s19
	s_waitcnt lgkmcnt(0)
	v_perm_b32 v240, v221, v220, s16
	v_perm_b32 v241, v221, v220, s17
	v_perm_b32 v242, v223, v222, s16
	v_perm_b32 v243, v223, v222, s17
	v_perm_b32 v227, v242, v240, s18
	v_perm_b32 v231, v242, v240, s19
	v_perm_b32 v235, v243, v241, s18
	v_perm_b32 v239, v243, v241, s19
	s_add_u32 s26, s8, 0x1000
	s_addc_u32 s27, s9, 0
	global_store_dwordx4 v249, v[224:227], s[8:9] sc1
	global_store_dwordx4 v249, v[228:231], s[8:9] offset:2048 sc1
	global_store_dwordx4 v249, v[232:235], s[26:27] sc1
	global_store_dwordx4 v249, v[236:239], s[26:27] offset:2048 sc1
	s_mov_b64 s[8:9], s[20:21]
	s_waitcnt vmcnt(40)
	v_mul_f32_e32 v128, 0x42800000, v128
	v_mul_f32_e32 v129, 0x42800000, v129
	v_mul_f32_e32 v130, 0x42800000, v130
	v_mul_f32_e32 v131, 0x42800000, v131
	v_med3_f32 v128, v128, s15, v250
	v_med3_f32 v129, v129, s15, v250
	v_med3_f32 v130, v130, s15, v250
	v_med3_f32 v131, v131, s15, v250
	v_cvt_pk_fp8_f32 v192, v128, v129
	v_cvt_pk_fp8_f32 v192, v130, v131 op_sel:[0,0,1]
	v_mul_f32_e32 v132, 0x42800000, v132
	v_mul_f32_e32 v133, 0x42800000, v133
	v_mul_f32_e32 v134, 0x42800000, v134
	v_mul_f32_e32 v135, 0x42800000, v135
	v_med3_f32 v132, v132, s15, v250
	v_med3_f32 v133, v133, s15, v250
	v_med3_f32 v134, v134, s15, v250
	v_med3_f32 v135, v135, s15, v250
	v_cvt_pk_fp8_f32 v193, v132, v133
	v_cvt_pk_fp8_f32 v193, v134, v135 op_sel:[0,0,1]
	v_mul_f32_e32 v136, 0x42800000, v136
	v_mul_f32_e32 v137, 0x42800000, v137
	v_mul_f32_e32 v138, 0x42800000, v138
	v_mul_f32_e32 v139, 0x42800000, v139
	v_med3_f32 v136, v136, s15, v250
	v_med3_f32 v137, v137, s15, v250
	v_med3_f32 v138, v138, s15, v250
	v_med3_f32 v139, v139, s15, v250
	v_cvt_pk_fp8_f32 v194, v136, v137
	v_cvt_pk_fp8_f32 v194, v138, v139 op_sel:[0,0,1]
	v_mul_f32_e32 v140, 0x42800000, v140
	v_mul_f32_e32 v141, 0x42800000, v141
	v_mul_f32_e32 v142, 0x42800000, v142
	v_mul_f32_e32 v143, 0x42800000, v143
	v_med3_f32 v140, v140, s15, v250
	v_med3_f32 v141, v141, s15, v250
	v_med3_f32 v142, v142, s15, v250
	v_med3_f32 v143, v143, s15, v250
	v_cvt_pk_fp8_f32 v195, v140, v141
	v_cvt_pk_fp8_f32 v195, v142, v143 op_sel:[0,0,1]
	v_mul_f32_e32 v144, 0x42800000, v144
	v_mul_f32_e32 v145, 0x42800000, v145
	v_mul_f32_e32 v146, 0x42800000, v146
	v_mul_f32_e32 v147, 0x42800000, v147
	v_med3_f32 v144, v144, s15, v250
	v_med3_f32 v145, v145, s15, v250
	v_med3_f32 v146, v146, s15, v250
	v_med3_f32 v147, v147, s15, v250
	v_cvt_pk_fp8_f32 v196, v144, v145
	v_cvt_pk_fp8_f32 v196, v146, v147 op_sel:[0,0,1]
	v_mul_f32_e32 v148, 0x42800000, v148
	v_mul_f32_e32 v149, 0x42800000, v149
	v_mul_f32_e32 v150, 0x42800000, v150
	v_mul_f32_e32 v151, 0x42800000, v151
	v_med3_f32 v148, v148, s15, v250
	v_med3_f32 v149, v149, s15, v250
	v_med3_f32 v150, v150, s15, v250
	v_med3_f32 v151, v151, s15, v250
	v_cvt_pk_fp8_f32 v197, v148, v149
	v_cvt_pk_fp8_f32 v197, v150, v151 op_sel:[0,0,1]
	v_mul_f32_e32 v152, 0x42800000, v152
	v_mul_f32_e32 v153, 0x42800000, v153
	v_mul_f32_e32 v154, 0x42800000, v154
	v_mul_f32_e32 v155, 0x42800000, v155
	v_med3_f32 v152, v152, s15, v250
	v_med3_f32 v153, v153, s15, v250
	v_med3_f32 v154, v154, s15, v250
	v_med3_f32 v155, v155, s15, v250
	v_cvt_pk_fp8_f32 v198, v152, v153
	v_cvt_pk_fp8_f32 v198, v154, v155 op_sel:[0,0,1]
	v_mul_f32_e32 v156, 0x42800000, v156
	v_mul_f32_e32 v157, 0x42800000, v157
	v_mul_f32_e32 v158, 0x42800000, v158
	v_mul_f32_e32 v159, 0x42800000, v159
	v_med3_f32 v156, v156, s15, v250
	v_med3_f32 v157, v157, s15, v250
	v_med3_f32 v158, v158, s15, v250
	v_med3_f32 v159, v159, s15, v250
	v_cvt_pk_fp8_f32 v199, v156, v157
	v_cvt_pk_fp8_f32 v199, v158, v159 op_sel:[0,0,1]
	v_mul_f32_e32 v160, 0x42800000, v160
	v_mul_f32_e32 v161, 0x42800000, v161
	v_mul_f32_e32 v162, 0x42800000, v162
	v_mul_f32_e32 v163, 0x42800000, v163
	v_med3_f32 v160, v160, s15, v250
	v_med3_f32 v161, v161, s15, v250
	v_med3_f32 v162, v162, s15, v250
	v_med3_f32 v163, v163, s15, v250
	v_cvt_pk_fp8_f32 v200, v160, v161
	v_cvt_pk_fp8_f32 v200, v162, v163 op_sel:[0,0,1]
	v_mul_f32_e32 v164, 0x42800000, v164
	v_mul_f32_e32 v165, 0x42800000, v165
	v_mul_f32_e32 v166, 0x42800000, v166
	v_mul_f32_e32 v167, 0x42800000, v167
	v_med3_f32 v164, v164, s15, v250
	v_med3_f32 v165, v165, s15, v250
	v_med3_f32 v166, v166, s15, v250
	v_med3_f32 v167, v167, s15, v250
	v_cvt_pk_fp8_f32 v201, v164, v165
	v_cvt_pk_fp8_f32 v201, v166, v167 op_sel:[0,0,1]
	v_mul_f32_e32 v168, 0x42800000, v168
	v_mul_f32_e32 v169, 0x42800000, v169
	v_mul_f32_e32 v170, 0x42800000, v170
	v_mul_f32_e32 v171, 0x42800000, v171
	v_med3_f32 v168, v168, s15, v250
	v_med3_f32 v169, v169, s15, v250
	v_med3_f32 v170, v170, s15, v250
	v_med3_f32 v171, v171, s15, v250
	v_cvt_pk_fp8_f32 v202, v168, v169
	v_cvt_pk_fp8_f32 v202, v170, v171 op_sel:[0,0,1]
	v_mul_f32_e32 v172, 0x42800000, v172
	v_mul_f32_e32 v173, 0x42800000, v173
	v_mul_f32_e32 v174, 0x42800000, v174
	v_mul_f32_e32 v175, 0x42800000, v175
	v_med3_f32 v172, v172, s15, v250
	v_med3_f32 v173, v173, s15, v250
	v_med3_f32 v174, v174, s15, v250
	v_med3_f32 v175, v175, s15, v250
	v_cvt_pk_fp8_f32 v203, v172, v173
	v_cvt_pk_fp8_f32 v203, v174, v175 op_sel:[0,0,1]
	v_mul_f32_e32 v176, 0x42800000, v176
	v_mul_f32_e32 v177, 0x42800000, v177
	v_mul_f32_e32 v178, 0x42800000, v178
	v_mul_f32_e32 v179, 0x42800000, v179
	v_med3_f32 v176, v176, s15, v250
	v_med3_f32 v177, v177, s15, v250
	v_med3_f32 v178, v178, s15, v250
	v_med3_f32 v179, v179, s15, v250
	v_cvt_pk_fp8_f32 v204, v176, v177
	v_cvt_pk_fp8_f32 v204, v178, v179 op_sel:[0,0,1]
	v_mul_f32_e32 v180, 0x42800000, v180
	v_mul_f32_e32 v181, 0x42800000, v181
	v_mul_f32_e32 v182, 0x42800000, v182
	v_mul_f32_e32 v183, 0x42800000, v183
	v_med3_f32 v180, v180, s15, v250
	v_med3_f32 v181, v181, s15, v250
	v_med3_f32 v182, v182, s15, v250
	v_med3_f32 v183, v183, s15, v250
	v_cvt_pk_fp8_f32 v205, v180, v181
	v_cvt_pk_fp8_f32 v205, v182, v183 op_sel:[0,0,1]
	v_mul_f32_e32 v184, 0x42800000, v184
	v_mul_f32_e32 v185, 0x42800000, v185
	v_mul_f32_e32 v186, 0x42800000, v186
	v_mul_f32_e32 v187, 0x42800000, v187
	v_med3_f32 v184, v184, s15, v250
	v_med3_f32 v185, v185, s15, v250
	v_med3_f32 v186, v186, s15, v250
	v_med3_f32 v187, v187, s15, v250
	v_cvt_pk_fp8_f32 v206, v184, v185
	v_cvt_pk_fp8_f32 v206, v186, v187 op_sel:[0,0,1]
	v_mul_f32_e32 v188, 0x42800000, v188
	v_mul_f32_e32 v189, 0x42800000, v189
	v_mul_f32_e32 v190, 0x42800000, v190
	v_mul_f32_e32 v191, 0x42800000, v191
	v_med3_f32 v188, v188, s15, v250
	v_med3_f32 v189, v189, s15, v250
	v_med3_f32 v190, v190, s15, v250
	v_med3_f32 v191, v191, s15, v250
	v_cvt_pk_fp8_f32 v207, v188, v189
	v_cvt_pk_fp8_f32 v207, v190, v191 op_sel:[0,0,1]
	s_min_u32 s22, s2, s28
	s_cmp_lt_u32 s22, 0x10000
	s_cbranch_scc0 .Lcv_dn_5
	s_lshr_b32 s23, s22, 11
	s_bfe_u32 s24, s22, 0x40007
	s_and_b32 s25, s22, 0x7f
	s_lshl_b32 s30, s24, 7
	s_lshl_b32 s24, s24, 21
	s_lshl_b32 s22, s25, 7
	s_add_u32 s24, s24, s22
	s_lshl_b32 s25, s25, 16
	s_add_u32 s30, s30, s25
	s_lshl_b32 s22, s23, 25
	s_add_u32 s24, s24, s22
	s_add_u32 s4, s70, s24
	s_addc_u32 s5, s71, 0
	s_lshl_b32 s23, s23, 23
	s_add_u32 s30, s30, s23
	s_add_u32 s30, s30, 0x38ee1c00
	s_add_u32 s20, s92, s30
	s_addc_u32 s21, s93, 0
	s_mov_b32 s14, 0x20000
	s_mov_b64 vcc, -1
	s_branch .Lcv_ld_5

.Lcv_ld_5:
	s_add_u32 s2, s2, s3
	v_cndmask_b32_e32 v246, v245, v244, vcc
	global_load_dwordx4 v[128:131], v246, s[4:5] nt
	s_add_u32 s4, s4, s14
	s_addc_u32 s5, s5, 0
	global_load_dwordx4 v[132:135], v246, s[4:5] nt
	s_add_u32 s4, s4, s14
	s_addc_u32 s5, s5, 0
	global_load_dwordx4 v[136:139], v246, s[4:5] nt
	s_add_u32 s4, s4, s14
	s_addc_u32 s5, s5, 0
	global_load_dwordx4 v[140:143], v246, s[4:5] nt
	s_add_u32 s4, s4, s14
	s_addc_u32 s5, s5, 0
	global_load_dwordx4 v[144:147], v246, s[4:5] nt
	s_add_u32 s4, s4, s14
	s_addc_u32 s5, s5, 0
	global_load_dwordx4 v[148:151], v246, s[4:5] nt
	s_add_u32 s4, s4, s14
	s_addc_u32 s5, s5, 0
	global_load_dwordx4 v[152:155], v246, s[4:5] nt
	s_add_u32 s4, s4, s14
	s_addc_u32 s5, s5, 0
	global_load_dwordx4 v[156:159], v246, s[4:5] nt
	s_add_u32 s4, s4, s14
	s_addc_u32 s5, s5, 0
	global_load_dwordx4 v[160:163], v246, s[4:5] nt
	s_add_u32 s4, s4, s14
	s_addc_u32 s5, s5, 0
	global_load_dwordx4 v[164:167], v246, s[4:5] nt
	s_add_u32 s4, s4, s14
	s_addc_u32 s5, s5, 0
	global_load_dwordx4 v[168:171], v246, s[4:5] nt
	s_add_u32 s4, s4, s14
	s_addc_u32 s5, s5, 0
	global_load_dwordx4 v[172:175], v246, s[4:5] nt
	s_add_u32 s4, s4, s14
	s_addc_u32 s5, s5, 0
	global_load_dwordx4 v[176:179], v246, s[4:5] nt
	s_add_u32 s4, s4, s14
	s_addc_u32 s5, s5, 0
	global_load_dwordx4 v[180:183], v246, s[4:5] nt
	s_add_u32 s4, s4, s14
	s_addc_u32 s5, s5, 0
	global_load_dwordx4 v[184:187], v246, s[4:5] nt
	s_add_u32 s4, s4, s14
	s_addc_u32 s5, s5, 0
	global_load_dwordx4 v[188:191], v246, s[4:5] nt
	ds_write_b32 v247, v192 offset:0
	ds_write_b32 v247, v193 offset:32
	ds_write_b32 v247, v194 offset:64
	ds_write_b32 v247, v195 offset:96
	ds_write_b32 v247, v196 offset:128
	ds_write_b32 v247, v197 offset:160
	ds_write_b32 v247, v198 offset:192
	ds_write_b32 v247, v199 offset:224
	ds_write_b32 v247, v200 offset:256
	ds_write_b32 v247, v201 offset:288
	ds_write_b32 v247, v202 offset:320
	ds_write_b32 v247, v203 offset:352
	ds_write_b32 v247, v204 offset:384
	ds_write_b32 v247, v205 offset:416
	ds_write_b32 v247, v206 offset:448
	ds_write_b32 v247, v207 offset:480
	ds_read_b128 v[208:211], v248 offset:0
	ds_read_b128 v[212:215], v248 offset:16
	ds_read_b128 v[216:219], v248 offset:32
	ds_read_b128 v[220:223], v248 offset:48
	s_waitcnt lgkmcnt(3)
	v_perm_b32 v240, v209, v208, s16
	v_perm_b32 v241, v209, v208, s17
	v_perm_b32 v242, v211, v210, s16
	v_perm_b32 v243, v211, v210, s17
	v_perm_b32 v224, v242, v240, s18
	v_perm_b32 v228, v242, v240, s19
	v_perm_b32 v232, v243, v241, s18
	v_perm_b32 v236, v243, v241, s19
	s_waitcnt lgkmcnt(2)
	v_perm_b32 v240, v213, v212, s16
	v_perm_b32 v241, v213, v212, s17
	v_perm_b32 v242, v215, v214, s16
	v_perm_b32 v243, v215, v214, s17
	v_perm_b32 v225, v242, v240, s18
	v_perm_b32 v229, v242, v240, s19
	v_perm_b32 v233, v243, v241, s18
	v_perm_b32 v237, v243, v241, s19
	s_waitcnt lgkmcnt(1)
	v_perm_b32 v240, v217, v216, s16
	v_perm_b32 v241, v217, v216, s17
	v_perm_b32 v242, v219, v218, s16
	v_perm_b32 v243, v219, v218, s17
	v_perm_b32 v226, v242, v240, s18
	v_perm_b32 v230, v242, v240, s19
	v_perm_b32 v234, v243, v241, s18
	v_perm_b32 v238, v243, v241, s19
	s_waitcnt lgkmcnt(0)
	v_perm_b32 v240, v221, v220, s16
	v_perm_b32 v241, v221, v220, s17
	v_perm_b32 v242, v223, v222, s16
	v_perm_b32 v243, v223, v222, s17
	v_perm_b32 v227, v242, v240, s18
	v_perm_b32 v231, v242, v240, s19
	v_perm_b32 v235, v243, v241, s18
	v_perm_b32 v239, v243, v241, s19
	s_add_u32 s26, s10, 0x1000
	s_addc_u32 s27, s11, 0
	global_store_dwordx4 v249, v[224:227], s[10:11] sc1
	global_store_dwordx4 v249, v[228:231], s[10:11] offset:2048 sc1
	global_store_dwordx4 v249, v[232:235], s[26:27] sc1
	global_store_dwordx4 v249, v[236:239], s[26:27] offset:2048 sc1
	s_mov_b64 s[10:11], s[20:21]
	s_sub_u32 s22, s2, s31
	s_cmp_gt_u32 s22, s28
	s_cbranch_scc1 .Lcv_done

.Lcv_ld_6:
	s_add_u32 s2, s2, s3
	v_cndmask_b32_e32 v246, v245, v244, vcc
	global_load_dwordx4 v[0:3], v246, s[4:5] nt
	s_add_u32 s4, s4, s14
	s_addc_u32 s5, s5, 0
	global_load_dwordx4 v[4:7], v246, s[4:5] nt
	s_add_u32 s4, s4, s14
	s_addc_u32 s5, s5, 0
	global_load_dwordx4 v[8:11], v246, s[4:5] nt
	s_add_u32 s4, s4, s14
	s_addc_u32 s5, s5, 0
	global_load_dwordx4 v[12:15], v246, s[4:5] nt
	s_add_u32 s4, s4, s14
	s_addc_u32 s5, s5, 0
	global_load_dwordx4 v[16:19], v246, s[4:5] nt
	s_add_u32 s4, s4, s14
	s_addc_u32 s5, s5, 0
	global_load_dwordx4 v[20:23], v246, s[4:5] nt
	s_add_u32 s4, s4, s14
	s_addc_u32 s5, s5, 0
	global_load_dwordx4 v[24:27], v246, s[4:5] nt
	s_add_u32 s4, s4, s14
	s_addc_u32 s5, s5, 0
	global_load_dwordx4 v[28:31], v246, s[4:5] nt
	s_add_u32 s4, s4, s14
	s_addc_u32 s5, s5, 0
	global_load_dwordx4 v[32:35], v246, s[4:5] nt
	s_add_u32 s4, s4, s14
	s_addc_u32 s5, s5, 0
	global_load_dwordx4 v[36:39], v246, s[4:5] nt
	s_add_u32 s4, s4, s14
	s_addc_u32 s5, s5, 0
	global_load_dwordx4 v[40:43], v246, s[4:5] nt
	s_add_u32 s4, s4, s14
	s_addc_u32 s5, s5, 0
	global_load_dwordx4 v[44:47], v246, s[4:5] nt
	s_add_u32 s4, s4, s14
	s_addc_u32 s5, s5, 0
	global_load_dwordx4 v[48:51], v246, s[4:5] nt
	s_add_u32 s4, s4, s14
	s_addc_u32 s5, s5, 0
	global_load_dwordx4 v[52:55], v246, s[4:5] nt
	s_add_u32 s4, s4, s14
	s_addc_u32 s5, s5, 0
	global_load_dwordx4 v[56:59], v246, s[4:5] nt
	s_add_u32 s4, s4, s14
	s_addc_u32 s5, s5, 0
	global_load_dwordx4 v[60:63], v246, s[4:5] nt
	ds_write_b32 v247, v192 offset:0
	ds_write_b32 v247, v193 offset:32
	ds_write_b32 v247, v194 offset:64
	ds_write_b32 v247, v195 offset:96
	ds_write_b32 v247, v196 offset:128
	ds_write_b32 v247, v197 offset:160
	ds_write_b32 v247, v198 offset:192
	ds_write_b32 v247, v199 offset:224
	ds_write_b32 v247, v200 offset:256
	ds_write_b32 v247, v201 offset:288
	ds_write_b32 v247, v202 offset:320
	ds_write_b32 v247, v203 offset:352
	ds_write_b32 v247, v204 offset:384
	ds_write_b32 v247, v205 offset:416
	ds_write_b32 v247, v206 offset:448
	ds_write_b32 v247, v207 offset:480
	ds_read_b128 v[208:211], v248 offset:0
	ds_read_b128 v[212:215], v248 offset:16
	ds_read_b128 v[216:219], v248 offset:32
	ds_read_b128 v[220:223], v248 offset:48
	s_waitcnt lgkmcnt(3)
	v_perm_b32 v240, v209, v208, s16
	v_perm_b32 v241, v209, v208, s17
	v_perm_b32 v242, v211, v210, s16
	v_perm_b32 v243, v211, v210, s17
	v_perm_b32 v224, v242, v240, s18
	v_perm_b32 v228, v242, v240, s19
	v_perm_b32 v232, v243, v241, s18
	v_perm_b32 v236, v243, v241, s19
	s_waitcnt lgkmcnt(2)
	v_perm_b32 v240, v213, v212, s16
	v_perm_b32 v241, v213, v212, s17
	v_perm_b32 v242, v215, v214, s16
	v_perm_b32 v243, v215, v214, s17
	v_perm_b32 v225, v242, v240, s18
	v_perm_b32 v229, v242, v240, s19
	v_perm_b32 v233, v243, v241, s18
	v_perm_b32 v237, v243, v241, s19
	s_waitcnt lgkmcnt(1)
	v_perm_b32 v240, v217, v216, s16
	v_perm_b32 v241, v217, v216, s17
	v_perm_b32 v242, v219, v218, s16
	v_perm_b32 v243, v219, v218, s17
	v_perm_b32 v226, v242, v240, s18
	v_perm_b32 v230, v242, v240, s19
	v_perm_b32 v234, v243, v241, s18
	v_perm_b32 v238, v243, v241, s19
	s_waitcnt lgkmcnt(0)
	v_perm_b32 v240, v221, v220, s16
	v_perm_b32 v241, v221, v220, s17
	v_perm_b32 v242, v223, v222, s16
	v_perm_b32 v243, v223, v222, s17
	v_perm_b32 v227, v242, v240, s18
	v_perm_b32 v231, v242, v240, s19
	v_perm_b32 v235, v243, v241, s18
	v_perm_b32 v239, v243, v241, s19
	s_add_u32 s26, s6, 0x1000
	s_addc_u32 s27, s7, 0
	global_store_dwordx4 v249, v[224:227], s[6:7] sc1
	global_store_dwordx4 v249, v[228:231], s[6:7] offset:2048 sc1
	global_store_dwordx4 v249, v[232:235], s[26:27] sc1
	global_store_dwordx4 v249, v[236:239], s[26:27] offset:2048 sc1
	s_mov_b64 s[6:7], s[20:21]
	s_waitcnt vmcnt(44)
	v_mul_f32_e32 v64, 0x42800000, v64
	v_mul_f32_e32 v65, 0x42800000, v65
	v_mul_f32_e32 v66, 0x42800000, v66
	v_mul_f32_e32 v67, 0x42800000, v67
	v_med3_f32 v64, v64, s15, v250
	v_med3_f32 v65, v65, s15, v250
	v_med3_f32 v66, v66, s15, v250
	v_med3_f32 v67, v67, s15, v250
	v_cvt_pk_fp8_f32 v192, v64, v65
	v_cvt_pk_fp8_f32 v192, v66, v67 op_sel:[0,0,1]
	v_mul_f32_e32 v68, 0x42800000, v68
	v_mul_f32_e32 v69, 0x42800000, v69
	v_mul_f32_e32 v70, 0x42800000, v70
	v_mul_f32_e32 v71, 0x42800000, v71
	v_med3_f32 v68, v68, s15, v250
	v_med3_f32 v69, v69, s15, v250
	v_med3_f32 v70, v70, s15, v250
	v_med3_f32 v71, v71, s15, v250
	v_cvt_pk_fp8_f32 v193, v68, v69
	v_cvt_pk_fp8_f32 v193, v70, v71 op_sel:[0,0,1]
	v_mul_f32_e32 v72, 0x42800000, v72
	v_mul_f32_e32 v73, 0x42800000, v73
	v_mul_f32_e32 v74, 0x42800000, v74
	v_mul_f32_e32 v75, 0x42800000, v75
	v_med3_f32 v72, v72, s15, v250
	v_med3_f32 v73, v73, s15, v250
	v_med3_f32 v74, v74, s15, v250
	v_med3_f32 v75, v75, s15, v250
	v_cvt_pk_fp8_f32 v194, v72, v73
	v_cvt_pk_fp8_f32 v194, v74, v75 op_sel:[0,0,1]
	v_mul_f32_e32 v76, 0x42800000, v76
	v_mul_f32_e32 v77, 0x42800000, v77
	v_mul_f32_e32 v78, 0x42800000, v78
	v_mul_f32_e32 v79, 0x42800000, v79
	v_med3_f32 v76, v76, s15, v250
	v_med3_f32 v77, v77, s15, v250
	v_med3_f32 v78, v78, s15, v250
	v_med3_f32 v79, v79, s15, v250
	v_cvt_pk_fp8_f32 v195, v76, v77
	v_cvt_pk_fp8_f32 v195, v78, v79 op_sel:[0,0,1]
	v_mul_f32_e32 v80, 0x42800000, v80
	v_mul_f32_e32 v81, 0x42800000, v81
	v_mul_f32_e32 v82, 0x42800000, v82
	v_mul_f32_e32 v83, 0x42800000, v83
	v_med3_f32 v80, v80, s15, v250
	v_med3_f32 v81, v81, s15, v250
	v_med3_f32 v82, v82, s15, v250
	v_med3_f32 v83, v83, s15, v250
	v_cvt_pk_fp8_f32 v196, v80, v81
	v_cvt_pk_fp8_f32 v196, v82, v83 op_sel:[0,0,1]
	v_mul_f32_e32 v84, 0x42800000, v84
	v_mul_f32_e32 v85, 0x42800000, v85
	v_mul_f32_e32 v86, 0x42800000, v86
	v_mul_f32_e32 v87, 0x42800000, v87
	v_med3_f32 v84, v84, s15, v250
	v_med3_f32 v85, v85, s15, v250
	v_med3_f32 v86, v86, s15, v250
	v_med3_f32 v87, v87, s15, v250
	v_cvt_pk_fp8_f32 v197, v84, v85
	v_cvt_pk_fp8_f32 v197, v86, v87 op_sel:[0,0,1]
	v_mul_f32_e32 v88, 0x42800000, v88
	v_mul_f32_e32 v89, 0x42800000, v89
	v_mul_f32_e32 v90, 0x42800000, v90
	v_mul_f32_e32 v91, 0x42800000, v91
	v_med3_f32 v88, v88, s15, v250
	v_med3_f32 v89, v89, s15, v250
	v_med3_f32 v90, v90, s15, v250
	v_med3_f32 v91, v91, s15, v250
	v_cvt_pk_fp8_f32 v198, v88, v89
	v_cvt_pk_fp8_f32 v198, v90, v91 op_sel:[0,0,1]
	v_mul_f32_e32 v92, 0x42800000, v92
	v_mul_f32_e32 v93, 0x42800000, v93
	v_mul_f32_e32 v94, 0x42800000, v94
	v_mul_f32_e32 v95, 0x42800000, v95
	v_med3_f32 v92, v92, s15, v250
	v_med3_f32 v93, v93, s15, v250
	v_med3_f32 v94, v94, s15, v250
	v_med3_f32 v95, v95, s15, v250
	v_cvt_pk_fp8_f32 v199, v92, v93
	v_cvt_pk_fp8_f32 v199, v94, v95 op_sel:[0,0,1]
	v_mul_f32_e32 v96, 0x42800000, v96
	v_mul_f32_e32 v97, 0x42800000, v97
	v_mul_f32_e32 v98, 0x42800000, v98
	v_mul_f32_e32 v99, 0x42800000, v99
	v_med3_f32 v96, v96, s15, v250
	v_med3_f32 v97, v97, s15, v250
	v_med3_f32 v98, v98, s15, v250
	v_med3_f32 v99, v99, s15, v250
	v_cvt_pk_fp8_f32 v200, v96, v97
	v_cvt_pk_fp8_f32 v200, v98, v99 op_sel:[0,0,1]
	v_mul_f32_e32 v100, 0x42800000, v100
	v_mul_f32_e32 v101, 0x42800000, v101
	v_mul_f32_e32 v102, 0x42800000, v102
	v_mul_f32_e32 v103, 0x42800000, v103
	v_med3_f32 v100, v100, s15, v250
	v_med3_f32 v101, v101, s15, v250
	v_med3_f32 v102, v102, s15, v250
	v_med3_f32 v103, v103, s15, v250
	v_cvt_pk_fp8_f32 v201, v100, v101
	v_cvt_pk_fp8_f32 v201, v102, v103 op_sel:[0,0,1]
	v_mul_f32_e32 v104, 0x42800000, v104
	v_mul_f32_e32 v105, 0x42800000, v105
	v_mul_f32_e32 v106, 0x42800000, v106
	v_mul_f32_e32 v107, 0x42800000, v107
	v_med3_f32 v104, v104, s15, v250
	v_med3_f32 v105, v105, s15, v250
	v_med3_f32 v106, v106, s15, v250
	v_med3_f32 v107, v107, s15, v250
	v_cvt_pk_fp8_f32 v202, v104, v105
	v_cvt_pk_fp8_f32 v202, v106, v107 op_sel:[0,0,1]
	v_mul_f32_e32 v108, 0x42800000, v108
	v_mul_f32_e32 v109, 0x42800000, v109
	v_mul_f32_e32 v110, 0x42800000, v110
	v_mul_f32_e32 v111, 0x42800000, v111
	v_med3_f32 v108, v108, s15, v250
	v_med3_f32 v109, v109, s15, v250
	v_med3_f32 v110, v110, s15, v250
	v_med3_f32 v111, v111, s15, v250
	v_cvt_pk_fp8_f32 v203, v108, v109
	v_cvt_pk_fp8_f32 v203, v110, v111 op_sel:[0,0,1]
	v_mul_f32_e32 v112, 0x42800000, v112
	v_mul_f32_e32 v113, 0x42800000, v113
	v_mul_f32_e32 v114, 0x42800000, v114
	v_mul_f32_e32 v115, 0x42800000, v115
	v_med3_f32 v112, v112, s15, v250
	v_med3_f32 v113, v113, s15, v250
	v_med3_f32 v114, v114, s15, v250
	v_med3_f32 v115, v115, s15, v250
	v_cvt_pk_fp8_f32 v204, v112, v113
	v_cvt_pk_fp8_f32 v204, v114, v115 op_sel:[0,0,1]
	v_mul_f32_e32 v116, 0x42800000, v116
	v_mul_f32_e32 v117, 0x42800000, v117
	v_mul_f32_e32 v118, 0x42800000, v118
	v_mul_f32_e32 v119, 0x42800000, v119
	v_med3_f32 v116, v116, s15, v250
	v_med3_f32 v117, v117, s15, v250
	v_med3_f32 v118, v118, s15, v250
	v_med3_f32 v119, v119, s15, v250
	v_cvt_pk_fp8_f32 v205, v116, v117
	v_cvt_pk_fp8_f32 v205, v118, v119 op_sel:[0,0,1]
	v_mul_f32_e32 v120, 0x42800000, v120
	v_mul_f32_e32 v121, 0x42800000, v121
	v_mul_f32_e32 v122, 0x42800000, v122
	v_mul_f32_e32 v123, 0x42800000, v123
	v_med3_f32 v120, v120, s15, v250
	v_med3_f32 v121, v121, s15, v250
	v_med3_f32 v122, v122, s15, v250
	v_med3_f32 v123, v123, s15, v250
	v_cvt_pk_fp8_f32 v206, v120, v121
	v_cvt_pk_fp8_f32 v206, v122, v123 op_sel:[0,0,1]
	v_mul_f32_e32 v124, 0x42800000, v124
	v_mul_f32_e32 v125, 0x42800000, v125
	v_mul_f32_e32 v126, 0x42800000, v126
	v_mul_f32_e32 v127, 0x42800000, v127
	v_med3_f32 v124, v124, s15, v250
	v_med3_f32 v125, v125, s15, v250
	v_med3_f32 v126, v126, s15, v250
	v_med3_f32 v127, v127, s15, v250
	v_cvt_pk_fp8_f32 v207, v124, v125
	v_cvt_pk_fp8_f32 v207, v126, v127 op_sel:[0,0,1]
	s_min_u32 s22, s2, s28
	s_cmp_lt_u32 s22, 0x10000
	s_cbranch_scc0 .Lcv_dn_7
	s_lshr_b32 s23, s22, 11
	s_bfe_u32 s24, s22, 0x40007
	s_and_b32 s25, s22, 0x7f
	s_lshl_b32 s30, s24, 7
	s_lshl_b32 s24, s24, 21
	s_lshl_b32 s22, s25, 7
	s_add_u32 s24, s24, s22
	s_lshl_b32 s25, s25, 16
	s_add_u32 s30, s30, s25
	s_lshl_b32 s22, s23, 25
	s_add_u32 s24, s24, s22
	s_add_u32 s4, s70, s24
	s_addc_u32 s5, s71, 0
	s_lshl_b32 s23, s23, 23
	s_add_u32 s30, s30, s23
	s_add_u32 s30, s30, 0x38ee1c00
	s_add_u32 s20, s92, s30
	s_addc_u32 s21, s93, 0
	s_mov_b32 s14, 0x20000
	s_mov_b64 vcc, -1
	s_branch .Lcv_ld_7

.Lcv_ld_7:
	s_add_u32 s2, s2, s3
	v_cndmask_b32_e32 v246, v245, v244, vcc
	global_load_dwordx4 v[64:67], v246, s[4:5] nt
	s_add_u32 s4, s4, s14
	s_addc_u32 s5, s5, 0
	global_load_dwordx4 v[68:71], v246, s[4:5] nt
	s_add_u32 s4, s4, s14
	s_addc_u32 s5, s5, 0
	global_load_dwordx4 v[72:75], v246, s[4:5] nt
	s_add_u32 s4, s4, s14
	s_addc_u32 s5, s5, 0
	global_load_dwordx4 v[76:79], v246, s[4:5] nt
	s_add_u32 s4, s4, s14
	s_addc_u32 s5, s5, 0
	global_load_dwordx4 v[80:83], v246, s[4:5] nt
	s_add_u32 s4, s4, s14
	s_addc_u32 s5, s5, 0
	global_load_dwordx4 v[84:87], v246, s[4:5] nt
	s_add_u32 s4, s4, s14
	s_addc_u32 s5, s5, 0
	global_load_dwordx4 v[88:91], v246, s[4:5] nt
	s_add_u32 s4, s4, s14
	s_addc_u32 s5, s5, 0
	global_load_dwordx4 v[92:95], v246, s[4:5] nt
	s_add_u32 s4, s4, s14
	s_addc_u32 s5, s5, 0
	global_load_dwordx4 v[96:99], v246, s[4:5] nt
	s_add_u32 s4, s4, s14
	s_addc_u32 s5, s5, 0
	global_load_dwordx4 v[100:103], v246, s[4:5] nt
	s_add_u32 s4, s4, s14
	s_addc_u32 s5, s5, 0
	global_load_dwordx4 v[104:107], v246, s[4:5] nt
	s_add_u32 s4, s4, s14
	s_addc_u32 s5, s5, 0
	global_load_dwordx4 v[108:111], v246, s[4:5] nt
	s_add_u32 s4, s4, s14
	s_addc_u32 s5, s5, 0
	global_load_dwordx4 v[112:115], v246, s[4:5] nt
	s_add_u32 s4, s4, s14
	s_addc_u32 s5, s5, 0
	global_load_dwordx4 v[116:119], v246, s[4:5] nt
	s_add_u32 s4, s4, s14
	s_addc_u32 s5, s5, 0
	global_load_dwordx4 v[120:123], v246, s[4:5] nt
	s_add_u32 s4, s4, s14
	s_addc_u32 s5, s5, 0
	global_load_dwordx4 v[124:127], v246, s[4:5] nt
	ds_write_b32 v247, v192 offset:0
	ds_write_b32 v247, v193 offset:32
	ds_write_b32 v247, v194 offset:64
	ds_write_b32 v247, v195 offset:96
	ds_write_b32 v247, v196 offset:128
	ds_write_b32 v247, v197 offset:160
	ds_write_b32 v247, v198 offset:192
	ds_write_b32 v247, v199 offset:224
	ds_write_b32 v247, v200 offset:256
	ds_write_b32 v247, v201 offset:288
	ds_write_b32 v247, v202 offset:320
	ds_write_b32 v247, v203 offset:352
	ds_write_b32 v247, v204 offset:384
	ds_write_b32 v247, v205 offset:416
	ds_write_b32 v247, v206 offset:448
	ds_write_b32 v247, v207 offset:480
	ds_read_b128 v[208:211], v248 offset:0
	ds_read_b128 v[212:215], v248 offset:16
	ds_read_b128 v[216:219], v248 offset:32
	ds_read_b128 v[220:223], v248 offset:48
	s_waitcnt lgkmcnt(3)
	v_perm_b32 v240, v209, v208, s16
	v_perm_b32 v241, v209, v208, s17
	v_perm_b32 v242, v211, v210, s16
	v_perm_b32 v243, v211, v210, s17
	v_perm_b32 v224, v242, v240, s18
	v_perm_b32 v228, v242, v240, s19
	v_perm_b32 v232, v243, v241, s18
	v_perm_b32 v236, v243, v241, s19
	s_waitcnt lgkmcnt(2)
	v_perm_b32 v240, v213, v212, s16
	v_perm_b32 v241, v213, v212, s17
	v_perm_b32 v242, v215, v214, s16
	v_perm_b32 v243, v215, v214, s17
	v_perm_b32 v225, v242, v240, s18
	v_perm_b32 v229, v242, v240, s19
	v_perm_b32 v233, v243, v241, s18
	v_perm_b32 v237, v243, v241, s19
	s_waitcnt lgkmcnt(1)
	v_perm_b32 v240, v217, v216, s16
	v_perm_b32 v241, v217, v216, s17
	v_perm_b32 v242, v219, v218, s16
	v_perm_b32 v243, v219, v218, s17
	v_perm_b32 v226, v242, v240, s18
	v_perm_b32 v230, v242, v240, s19
	v_perm_b32 v234, v243, v241, s18
	v_perm_b32 v238, v243, v241, s19
	s_waitcnt lgkmcnt(0)
	v_perm_b32 v240, v221, v220, s16
	v_perm_b32 v241, v221, v220, s17
	v_perm_b32 v242, v223, v222, s16
	v_perm_b32 v243, v223, v222, s17
	v_perm_b32 v227, v242, v240, s18
	v_perm_b32 v231, v242, v240, s19
	v_perm_b32 v235, v243, v241, s18
	v_perm_b32 v239, v243, v241, s19
	s_add_u32 s26, s8, 0x1000
	s_addc_u32 s27, s9, 0
	global_store_dwordx4 v249, v[224:227], s[8:9] sc1
	global_store_dwordx4 v249, v[228:231], s[8:9] offset:2048 sc1
	global_store_dwordx4 v249, v[232:235], s[26:27] sc1
	global_store_dwordx4 v249, v[236:239], s[26:27] offset:2048 sc1
	s_mov_b64 s[8:9], s[20:21]
	s_waitcnt vmcnt(44)
	v_mul_f32_e32 v128, 0x42800000, v128
	v_mul_f32_e32 v129, 0x42800000, v129
	v_mul_f32_e32 v130, 0x42800000, v130
	v_mul_f32_e32 v131, 0x42800000, v131
	v_med3_f32 v128, v128, s15, v250
	v_med3_f32 v129, v129, s15, v250
	v_med3_f32 v130, v130, s15, v250
	v_med3_f32 v131, v131, s15, v250
	v_cvt_pk_fp8_f32 v192, v128, v129
	v_cvt_pk_fp8_f32 v192, v130, v131 op_sel:[0,0,1]
	v_mul_f32_e32 v132, 0x42800000, v132
	v_mul_f32_e32 v133, 0x42800000, v133
	v_mul_f32_e32 v134, 0x42800000, v134
	v_mul_f32_e32 v135, 0x42800000, v135
	v_med3_f32 v132, v132, s15, v250
	v_med3_f32 v133, v133, s15, v250
	v_med3_f32 v134, v134, s15, v250
	v_med3_f32 v135, v135, s15, v250
	v_cvt_pk_fp8_f32 v193, v132, v133
	v_cvt_pk_fp8_f32 v193, v134, v135 op_sel:[0,0,1]
	v_mul_f32_e32 v136, 0x42800000, v136
	v_mul_f32_e32 v137, 0x42800000, v137
	v_mul_f32_e32 v138, 0x42800000, v138
	v_mul_f32_e32 v139, 0x42800000, v139
	v_med3_f32 v136, v136, s15, v250
	v_med3_f32 v137, v137, s15, v250
	v_med3_f32 v138, v138, s15, v250
	v_med3_f32 v139, v139, s15, v250
	v_cvt_pk_fp8_f32 v194, v136, v137
	v_cvt_pk_fp8_f32 v194, v138, v139 op_sel:[0,0,1]
	v_mul_f32_e32 v140, 0x42800000, v140
	v_mul_f32_e32 v141, 0x42800000, v141
	v_mul_f32_e32 v142, 0x42800000, v142
	v_mul_f32_e32 v143, 0x42800000, v143
	v_med3_f32 v140, v140, s15, v250
	v_med3_f32 v141, v141, s15, v250
	v_med3_f32 v142, v142, s15, v250
	v_med3_f32 v143, v143, s15, v250
	v_cvt_pk_fp8_f32 v195, v140, v141
	v_cvt_pk_fp8_f32 v195, v142, v143 op_sel:[0,0,1]
	v_mul_f32_e32 v144, 0x42800000, v144
	v_mul_f32_e32 v145, 0x42800000, v145
	v_mul_f32_e32 v146, 0x42800000, v146
	v_mul_f32_e32 v147, 0x42800000, v147
	v_med3_f32 v144, v144, s15, v250
	v_med3_f32 v145, v145, s15, v250
	v_med3_f32 v146, v146, s15, v250
	v_med3_f32 v147, v147, s15, v250
	v_cvt_pk_fp8_f32 v196, v144, v145
	v_cvt_pk_fp8_f32 v196, v146, v147 op_sel:[0,0,1]
	v_mul_f32_e32 v148, 0x42800000, v148
	v_mul_f32_e32 v149, 0x42800000, v149
	v_mul_f32_e32 v150, 0x42800000, v150
	v_mul_f32_e32 v151, 0x42800000, v151
	v_med3_f32 v148, v148, s15, v250
	v_med3_f32 v149, v149, s15, v250
	v_med3_f32 v150, v150, s15, v250
	v_med3_f32 v151, v151, s15, v250
	v_cvt_pk_fp8_f32 v197, v148, v149
	v_cvt_pk_fp8_f32 v197, v150, v151 op_sel:[0,0,1]
	v_mul_f32_e32 v152, 0x42800000, v152
	v_mul_f32_e32 v153, 0x42800000, v153
	v_mul_f32_e32 v154, 0x42800000, v154
	v_mul_f32_e32 v155, 0x42800000, v155
	v_med3_f32 v152, v152, s15, v250
	v_med3_f32 v153, v153, s15, v250
	v_med3_f32 v154, v154, s15, v250
	v_med3_f32 v155, v155, s15, v250
	v_cvt_pk_fp8_f32 v198, v152, v153
	v_cvt_pk_fp8_f32 v198, v154, v155 op_sel:[0,0,1]
	v_mul_f32_e32 v156, 0x42800000, v156
	v_mul_f32_e32 v157, 0x42800000, v157
	v_mul_f32_e32 v158, 0x42800000, v158
	v_mul_f32_e32 v159, 0x42800000, v159
	v_med3_f32 v156, v156, s15, v250
	v_med3_f32 v157, v157, s15, v250
	v_med3_f32 v158, v158, s15, v250
	v_med3_f32 v159, v159, s15, v250
	v_cvt_pk_fp8_f32 v199, v156, v157
	v_cvt_pk_fp8_f32 v199, v158, v159 op_sel:[0,0,1]
	v_mul_f32_e32 v160, 0x42800000, v160
	v_mul_f32_e32 v161, 0x42800000, v161
	v_mul_f32_e32 v162, 0x42800000, v162
	v_mul_f32_e32 v163, 0x42800000, v163
	v_med3_f32 v160, v160, s15, v250
	v_med3_f32 v161, v161, s15, v250
	v_med3_f32 v162, v162, s15, v250
	v_med3_f32 v163, v163, s15, v250
	v_cvt_pk_fp8_f32 v200, v160, v161
	v_cvt_pk_fp8_f32 v200, v162, v163 op_sel:[0,0,1]
	v_mul_f32_e32 v164, 0x42800000, v164
	v_mul_f32_e32 v165, 0x42800000, v165
	v_mul_f32_e32 v166, 0x42800000, v166
	v_mul_f32_e32 v167, 0x42800000, v167
	v_med3_f32 v164, v164, s15, v250
	v_med3_f32 v165, v165, s15, v250
	v_med3_f32 v166, v166, s15, v250
	v_med3_f32 v167, v167, s15, v250
	v_cvt_pk_fp8_f32 v201, v164, v165
	v_cvt_pk_fp8_f32 v201, v166, v167 op_sel:[0,0,1]
	v_mul_f32_e32 v168, 0x42800000, v168
	v_mul_f32_e32 v169, 0x42800000, v169
	v_mul_f32_e32 v170, 0x42800000, v170
	v_mul_f32_e32 v171, 0x42800000, v171
	v_med3_f32 v168, v168, s15, v250
	v_med3_f32 v169, v169, s15, v250
	v_med3_f32 v170, v170, s15, v250
	v_med3_f32 v171, v171, s15, v250
	v_cvt_pk_fp8_f32 v202, v168, v169
	v_cvt_pk_fp8_f32 v202, v170, v171 op_sel:[0,0,1]
	v_mul_f32_e32 v172, 0x42800000, v172
	v_mul_f32_e32 v173, 0x42800000, v173
	v_mul_f32_e32 v174, 0x42800000, v174
	v_mul_f32_e32 v175, 0x42800000, v175
	v_med3_f32 v172, v172, s15, v250
	v_med3_f32 v173, v173, s15, v250
	v_med3_f32 v174, v174, s15, v250
	v_med3_f32 v175, v175, s15, v250
	v_cvt_pk_fp8_f32 v203, v172, v173
	v_cvt_pk_fp8_f32 v203, v174, v175 op_sel:[0,0,1]
	v_mul_f32_e32 v176, 0x42800000, v176
	v_mul_f32_e32 v177, 0x42800000, v177
	v_mul_f32_e32 v178, 0x42800000, v178
	v_mul_f32_e32 v179, 0x42800000, v179
	v_med3_f32 v176, v176, s15, v250
	v_med3_f32 v177, v177, s15, v250
	v_med3_f32 v178, v178, s15, v250
	v_med3_f32 v179, v179, s15, v250
	v_cvt_pk_fp8_f32 v204, v176, v177
	v_cvt_pk_fp8_f32 v204, v178, v179 op_sel:[0,0,1]
	v_mul_f32_e32 v180, 0x42800000, v180
	v_mul_f32_e32 v181, 0x42800000, v181
	v_mul_f32_e32 v182, 0x42800000, v182
	v_mul_f32_e32 v183, 0x42800000, v183
	v_med3_f32 v180, v180, s15, v250
	v_med3_f32 v181, v181, s15, v250
	v_med3_f32 v182, v182, s15, v250
	v_med3_f32 v183, v183, s15, v250
	v_cvt_pk_fp8_f32 v205, v180, v181
	v_cvt_pk_fp8_f32 v205, v182, v183 op_sel:[0,0,1]
	v_mul_f32_e32 v184, 0x42800000, v184
	v_mul_f32_e32 v185, 0x42800000, v185
	v_mul_f32_e32 v186, 0x42800000, v186
	v_mul_f32_e32 v187, 0x42800000, v187
	v_med3_f32 v184, v184, s15, v250
	v_med3_f32 v185, v185, s15, v250
	v_med3_f32 v186, v186, s15, v250
	v_med3_f32 v187, v187, s15, v250
	v_cvt_pk_fp8_f32 v206, v184, v185
	v_cvt_pk_fp8_f32 v206, v186, v187 op_sel:[0,0,1]
	v_mul_f32_e32 v188, 0x42800000, v188
	v_mul_f32_e32 v189, 0x42800000, v189
	v_mul_f32_e32 v190, 0x42800000, v190
	v_mul_f32_e32 v191, 0x42800000, v191
	v_med3_f32 v188, v188, s15, v250
	v_med3_f32 v189, v189, s15, v250
	v_med3_f32 v190, v190, s15, v250
	v_med3_f32 v191, v191, s15, v250
	v_cvt_pk_fp8_f32 v207, v188, v189
	v_cvt_pk_fp8_f32 v207, v190, v191 op_sel:[0,0,1]
	s_min_u32 s22, s2, s28
	s_cmp_lt_u32 s22, 0x10000
	s_cbranch_scc0 .Lcv_dn_8
	s_lshr_b32 s23, s22, 11
	s_bfe_u32 s24, s22, 0x40007
	s_and_b32 s25, s22, 0x7f
	s_lshl_b32 s30, s24, 7
	s_lshl_b32 s24, s24, 21
	s_lshl_b32 s22, s25, 7
	s_add_u32 s24, s24, s22
	s_lshl_b32 s25, s25, 16
	s_add_u32 s30, s30, s25
	s_lshl_b32 s22, s23, 25
	s_add_u32 s24, s24, s22
	s_add_u32 s4, s70, s24
	s_addc_u32 s5, s71, 0
	s_lshl_b32 s23, s23, 23
	s_add_u32 s30, s30, s23
	s_add_u32 s30, s30, 0x38ee1c00
	s_add_u32 s20, s92, s30
	s_addc_u32 s21, s93, 0
	s_mov_b32 s14, 0x20000
	s_mov_b64 vcc, -1
	s_branch .Lcv_ld_8

.Lcv_ld_8:
	s_add_u32 s2, s2, s3
	v_cndmask_b32_e32 v246, v245, v244, vcc
	global_load_dwordx4 v[128:131], v246, s[4:5] nt
	s_add_u32 s4, s4, s14
	s_addc_u32 s5, s5, 0
	global_load_dwordx4 v[132:135], v246, s[4:5] nt
	s_add_u32 s4, s4, s14
	s_addc_u32 s5, s5, 0
	global_load_dwordx4 v[136:139], v246, s[4:5] nt
	s_add_u32 s4, s4, s14
	s_addc_u32 s5, s5, 0
	global_load_dwordx4 v[140:143], v246, s[4:5] nt
	s_add_u32 s4, s4, s14
	s_addc_u32 s5, s5, 0
	global_load_dwordx4 v[144:147], v246, s[4:5] nt
	s_add_u32 s4, s4, s14
	s_addc_u32 s5, s5, 0
	global_load_dwordx4 v[148:151], v246, s[4:5] nt
	s_add_u32 s4, s4, s14
	s_addc_u32 s5, s5, 0
	global_load_dwordx4 v[152:155], v246, s[4:5] nt
	s_add_u32 s4, s4, s14
	s_addc_u32 s5, s5, 0
	global_load_dwordx4 v[156:159], v246, s[4:5] nt
	s_add_u32 s4, s4, s14
	s_addc_u32 s5, s5, 0
	global_load_dwordx4 v[160:163], v246, s[4:5] nt
	s_add_u32 s4, s4, s14
	s_addc_u32 s5, s5, 0
	global_load_dwordx4 v[164:167], v246, s[4:5] nt
	s_add_u32 s4, s4, s14
	s_addc_u32 s5, s5, 0
	global_load_dwordx4 v[168:171], v246, s[4:5] nt
	s_add_u32 s4, s4, s14
	s_addc_u32 s5, s5, 0
	global_load_dwordx4 v[172:175], v246, s[4:5] nt
	s_add_u32 s4, s4, s14
	s_addc_u32 s5, s5, 0
	global_load_dwordx4 v[176:179], v246, s[4:5] nt
	s_add_u32 s4, s4, s14
	s_addc_u32 s5, s5, 0
	global_load_dwordx4 v[180:183], v246, s[4:5] nt
	s_add_u32 s4, s4, s14
	s_addc_u32 s5, s5, 0
	global_load_dwordx4 v[184:187], v246, s[4:5] nt
	s_add_u32 s4, s4, s14
	s_addc_u32 s5, s5, 0
	global_load_dwordx4 v[188:191], v246, s[4:5] nt
	ds_write_b32 v247, v192 offset:0
	ds_write_b32 v247, v193 offset:32
	ds_write_b32 v247, v194 offset:64
	ds_write_b32 v247, v195 offset:96
	ds_write_b32 v247, v196 offset:128
	ds_write_b32 v247, v197 offset:160
	ds_write_b32 v247, v198 offset:192
	ds_write_b32 v247, v199 offset:224
	ds_write_b32 v247, v200 offset:256
	ds_write_b32 v247, v201 offset:288
	ds_write_b32 v247, v202 offset:320
	ds_write_b32 v247, v203 offset:352
	ds_write_b32 v247, v204 offset:384
	ds_write_b32 v247, v205 offset:416
	ds_write_b32 v247, v206 offset:448
	ds_write_b32 v247, v207 offset:480
	ds_read_b128 v[208:211], v248 offset:0
	ds_read_b128 v[212:215], v248 offset:16
	ds_read_b128 v[216:219], v248 offset:32
	ds_read_b128 v[220:223], v248 offset:48
	s_waitcnt lgkmcnt(3)
	v_perm_b32 v240, v209, v208, s16
	v_perm_b32 v241, v209, v208, s17
	v_perm_b32 v242, v211, v210, s16
	v_perm_b32 v243, v211, v210, s17
	v_perm_b32 v224, v242, v240, s18
	v_perm_b32 v228, v242, v240, s19
	v_perm_b32 v232, v243, v241, s18
	v_perm_b32 v236, v243, v241, s19
	s_waitcnt lgkmcnt(2)
	v_perm_b32 v240, v213, v212, s16
	v_perm_b32 v241, v213, v212, s17
	v_perm_b32 v242, v215, v214, s16
	v_perm_b32 v243, v215, v214, s17
	v_perm_b32 v225, v242, v240, s18
	v_perm_b32 v229, v242, v240, s19
	v_perm_b32 v233, v243, v241, s18
	v_perm_b32 v237, v243, v241, s19
	s_waitcnt lgkmcnt(1)
	v_perm_b32 v240, v217, v216, s16
	v_perm_b32 v241, v217, v216, s17
	v_perm_b32 v242, v219, v218, s16
	v_perm_b32 v243, v219, v218, s17
	v_perm_b32 v226, v242, v240, s18
	v_perm_b32 v230, v242, v240, s19
	v_perm_b32 v234, v243, v241, s18
	v_perm_b32 v238, v243, v241, s19
	s_waitcnt lgkmcnt(0)
	v_perm_b32 v240, v221, v220, s16
	v_perm_b32 v241, v221, v220, s17
	v_perm_b32 v242, v223, v222, s16
	v_perm_b32 v243, v223, v222, s17
	v_perm_b32 v227, v242, v240, s18
	v_perm_b32 v231, v242, v240, s19
	v_perm_b32 v235, v243, v241, s18
	v_perm_b32 v239, v243, v241, s19
	s_add_u32 s26, s10, 0x1000
	s_addc_u32 s27, s11, 0
	global_store_dwordx4 v249, v[224:227], s[10:11] sc1
	global_store_dwordx4 v249, v[228:231], s[10:11] offset:2048 sc1
	global_store_dwordx4 v249, v[232:235], s[26:27] sc1
	global_store_dwordx4 v249, v[236:239], s[26:27] offset:2048 sc1
	s_mov_b64 s[10:11], s[20:21]
	s_sub_u32 s22, s2, s31
	s_cmp_le_u32 s22, s28
	s_cbranch_scc1 .Lcv_loop
